# speedup vs baseline: 1.0096x; 1.0096x over previous
.LBB1_6:
	s_or_b64 exec, exec, s[4:5]
	s_lshr_b32 s5, s3, 8
	s_lshl_b32 s16, s20, 12
	s_lshl_b32 s4, s5, 5
	s_add_i32 s35, s16, 0
	s_add_u32 s18, s6, 0x18000
	v_and_b32_e32 v2, 12, v2
	v_bfe_u32 v0, v0, 2, 2
	s_addc_u32 s19, s7, 0
	v_bitop3_b32 v0, v2, v1, v0 bitop3:0x36
	s_add_u32 s16, s14, 0x8000
	v_lshlrev_b32_e32 v100, 4, v0
	v_or_b32_e32 v0, s4, v5
	s_addc_u32 s17, s15, 0
	s_lshl_b32 s36, s5, 7
	v_lshl_add_u32 v101, v0, 9, 0
	v_lshl_or_b32 v0, v1, 4, s36
	v_add_u32_e32 v0, 0, v0
	v_add_u32_e32 v83, v101, v100
	s_waitcnt vmcnt(0)
	s_waitcnt lgkmcnt(0)
	s_barrier
	v_add_u32_e32 v80, 0x22000, v0
	ds_read_b128 v[84:87], v83
	ds_read_b128 v[0:3], v80
	ds_read_b128 v[4:7], v80 offset:32
	ds_read_b128 v[8:11], v80 offset:64
	ds_read_b128 v[12:15], v80 offset:96
	ds_read_b128 v[88:91], v83 offset:256
	s_waitcnt vmcnt(15) lgkmcnt(1)
	v_mfma_f32_32x32x16_bf16 v[0:15], v[84:87], v[68:71], v[0:15]
	v_xor_b32_e32 v102, 32, v100
	v_add_u32_e32 v84, v101, v102
	v_xor_b32_e32 v103, 64, v100
	v_add_u32_e32 v85, v101, v103
	v_xor_b32_e32 v104, 0x60, v100
	v_xor_b32_e32 v105, 0x80, v100
	v_xor_b32_e32 v106, 0xa0, v100
	s_waitcnt vmcnt(7) lgkmcnt(0)
	v_mfma_f32_32x32x16_bf16 v[0:15], v[88:91], v[76:79], v[0:15]
	ds_read_b128 v[86:89], v84
	ds_read_b128 v[90:93], v84 offset:256
	v_xor_b32_e32 v107, 0xe0, v100
	v_lshl_add_u32 v81, v81, 4, s35
	v_add_u32_e32 v81, 0x18000, v81
	v_lshl_add_u32 v82, s5, 11, v81
	s_add_u32 s36, s6, 0x1a000
	s_addc_u32 s37, s7, 0
	s_waitcnt lgkmcnt(1)
	v_mfma_f32_32x32x16_bf16 v[0:15], v[86:89], v[60:63], v[0:15]
	s_add_u32 s38, s6, 0x1c000
	s_addc_u32 s39, s7, 0
	s_add_u32 s6, s6, 0x1e000
	s_addc_u32 s7, s7, 0
	s_waitcnt vmcnt(6) lgkmcnt(0)
	v_mfma_f32_32x32x16_bf16 v[0:15], v[90:93], v[72:75], v[0:15]
	ds_read_b128 v[86:89], v85
	ds_read_b128 v[90:93], v85 offset:256
	s_waitcnt lgkmcnt(1)
	v_mfma_f32_32x32x16_bf16 v[0:15], v[86:89], v[52:55], v[0:15]
	v_add_u32_e32 v86, v101, v104
	v_add_u32_e32 v87, v101, v105
	s_waitcnt vmcnt(5) lgkmcnt(0)
	v_mfma_f32_32x32x16_bf16 v[0:15], v[90:93], v[64:67], v[0:15]
	ds_read_b128 v[88:91], v86
	ds_read_b128 v[92:95], v86 offset:256
	s_waitcnt lgkmcnt(1)
	v_mfma_f32_32x32x16_bf16 v[0:15], v[88:91], v[48:51], v[0:15]
	s_waitcnt vmcnt(4) lgkmcnt(0)
	v_mfma_f32_32x32x16_bf16 v[0:15], v[92:95], v[56:59], v[0:15]
	ds_read_b128 v[88:91], v87
	ds_read_b128 v[92:95], v87 offset:256
	s_waitcnt lgkmcnt(1)
	v_mfma_f32_32x32x16_bf16 v[0:15], v[88:91], v[36:39], v[0:15]
	v_add_u32_e32 v88, v101, v106
	v_add_u32_e32 v89, v101, v107
	s_waitcnt vmcnt(3) lgkmcnt(0)
	v_mfma_f32_32x32x16_bf16 v[0:15], v[92:95], v[44:47], v[0:15]
	ds_read_b128 v[90:93], v88
	ds_read_b128 v[94:97], v88 offset:256
	s_waitcnt lgkmcnt(1)
	v_mfma_f32_32x32x16_bf16 v[0:15], v[90:93], v[28:31], v[0:15]
	v_xor_b32_e32 v91, 0xc0, v100
	v_add_u32_e32 v90, v101, v91
	v_add_u32_e32 v101, 0x10000, v101
	v_add_u32_e32 v100, v101, v100
	v_add_u32_e32 v91, v101, v91
	s_waitcnt vmcnt(2) lgkmcnt(0)
	v_mfma_f32_32x32x16_bf16 v[0:15], v[94:97], v[40:43], v[0:15]
	ds_read_b128 v[92:95], v90
	ds_read_b128 v[96:99], v90 offset:256
	s_waitcnt lgkmcnt(1)
	v_mfma_f32_32x32x16_bf16 v[0:15], v[92:95], v[24:27], v[0:15]
	ds_read_b128 v[92:95], v89
	s_waitcnt vmcnt(1) lgkmcnt(1)
	v_mfma_f32_32x32x16_bf16 v[0:15], v[96:99], v[32:35], v[0:15]
	ds_read_b128 v[96:99], v89 offset:256
	s_waitcnt lgkmcnt(1)
	v_mfma_f32_32x32x16_bf16 v[0:15], v[92:95], v[20:23], v[0:15]
	s_waitcnt vmcnt(0) lgkmcnt(0)
	v_mfma_f32_32x32x16_bf16 v[0:15], v[96:99], v[16:19], v[0:15]
	s_nop 11
	v_cvt_pk_bf16_f32 v0, v0, v1
	v_cvt_pk_bf16_f32 v1, v2, v3
	v_cvt_pk_bf16_f32 v2, v4, v5
	v_cvt_pk_bf16_f32 v3, v6, v7
	v_cvt_pk_bf16_f32 v4, v8, v9
	v_cvt_pk_bf16_f32 v5, v10, v11
	v_cvt_pk_bf16_f32 v6, v12, v13
	v_cvt_pk_bf16_f32 v7, v14, v15
	ds_write_b128 v82, v[0:3]
	ds_write_b128 v82, v[4:7] offset:1024
	s_waitcnt lgkmcnt(0)
	s_barrier
	s_mov_b32 s5, m0
	s_mov_b32 m0, s21
	s_nop 0
	global_load_lds_dwordx4 v192, s[18:19]
	s_mov_b32 m0, s5
	s_nop 0
	s_mov_b32 s5, m0
	s_mov_b32 m0, s31
	s_nop 0
	global_load_lds_dwordx4 v192, s[36:37]
	s_mov_b32 m0, s5
	s_nop 0
	s_mov_b32 s5, m0
	s_mov_b32 m0, s33
	s_nop 0
	global_load_lds_dwordx4 v192, s[38:39]
	s_mov_b32 m0, s5
	s_nop 0
	s_mov_b32 s5, m0
	s_mov_b32 m0, s34
	s_nop 0
	global_load_lds_dwordx4 v192, s[6:7]
	s_mov_b32 m0, s5
	ds_read_b128 v[0:3], v80 offset:256
	ds_read2_b32 v[4:5], v80 offset0:72 offset1:73
	ds_read_b128 v[92:95], v83 offset:32768
	ds_read2_b32 v[6:7], v80 offset0:74 offset1:75
	ds_read2_b32 v[8:9], v80 offset0:80 offset1:81
	ds_read2_b32 v[10:11], v80 offset0:82 offset1:83
	ds_read2_b32 v[12:13], v80 offset0:88 offset1:89
	ds_read2_b32 v[14:15], v80 offset0:90 offset1:91
	ds_read_b128 v[96:99], v83 offset:33024
	s_waitcnt lgkmcnt(1)
	v_mfma_f32_32x32x16_bf16 v[0:15], v[92:95], v[68:71], v[0:15]
	s_add_u32 s6, s14, 0x2000
	s_addc_u32 s7, s15, 0
	s_add_u32 s18, s14, 0x4000
	s_addc_u32 s19, s15, 0
	s_add_u32 s34, s14, 0x6000
	s_addc_u32 s35, s15, 0
	s_waitcnt lgkmcnt(0)
	v_mfma_f32_32x32x16_bf16 v[0:15], v[96:99], v[76:79], v[0:15]
	ds_read_b128 v[92:95], v84 offset:32768
	ds_read_b128 v[96:99], v84 offset:33024
	s_waitcnt lgkmcnt(1)
	v_mfma_f32_32x32x16_bf16 v[0:15], v[92:95], v[60:63], v[0:15]
	s_waitcnt lgkmcnt(0)
	v_mfma_f32_32x32x16_bf16 v[0:15], v[96:99], v[72:75], v[0:15]
	ds_read_b128 v[92:95], v85 offset:32768
	ds_read_b128 v[96:99], v85 offset:33024
	s_waitcnt lgkmcnt(1)
	v_mfma_f32_32x32x16_bf16 v[0:15], v[92:95], v[52:55], v[0:15]
	s_waitcnt lgkmcnt(0)
	v_mfma_f32_32x32x16_bf16 v[0:15], v[96:99], v[64:67], v[0:15]
	ds_read_b128 v[92:95], v86 offset:32768
	ds_read_b128 v[96:99], v86 offset:33024
	s_waitcnt lgkmcnt(1)
	v_mfma_f32_32x32x16_bf16 v[0:15], v[92:95], v[48:51], v[0:15]
	s_waitcnt lgkmcnt(0)
	v_mfma_f32_32x32x16_bf16 v[0:15], v[96:99], v[56:59], v[0:15]
	ds_read_b128 v[92:95], v87 offset:32768
	ds_read_b128 v[96:99], v87 offset:33024
	s_waitcnt lgkmcnt(1)
	v_mfma_f32_32x32x16_bf16 v[0:15], v[92:95], v[36:39], v[0:15]
	s_waitcnt lgkmcnt(0)
	v_mfma_f32_32x32x16_bf16 v[0:15], v[96:99], v[44:47], v[0:15]
	ds_read_b128 v[92:95], v88 offset:32768
	ds_read_b128 v[96:99], v88 offset:33024
	s_waitcnt lgkmcnt(1)
	v_mfma_f32_32x32x16_bf16 v[0:15], v[92:95], v[28:31], v[0:15]
	s_waitcnt lgkmcnt(0)
	v_mfma_f32_32x32x16_bf16 v[0:15], v[96:99], v[40:43], v[0:15]
	ds_read_b128 v[92:95], v90 offset:32768
	ds_read_b128 v[96:99], v90 offset:33024
	s_waitcnt lgkmcnt(1)
	v_mfma_f32_32x32x16_bf16 v[0:15], v[92:95], v[24:27], v[0:15]
	ds_read_b128 v[92:95], v89 offset:32768
	s_waitcnt lgkmcnt(1)
	v_mfma_f32_32x32x16_bf16 v[0:15], v[96:99], v[32:35], v[0:15]
	ds_read_b128 v[96:99], v89 offset:33024
	ds_read_b128 v[128:131], v81
	ds_read_b128 v[132:135], v81 offset:1024
	ds_read_b128 v[136:139], v81 offset:2048
	ds_read_b128 v[140:143], v81 offset:3072
	s_waitcnt lgkmcnt(5)
	v_mfma_f32_32x32x16_bf16 v[0:15], v[92:95], v[20:23], v[0:15]
	s_waitcnt lgkmcnt(4)
	v_mfma_f32_32x32x16_bf16 v[0:15], v[96:99], v[16:19], v[0:15]
	s_nop 11
	v_cvt_pk_bf16_f32 v0, v0, v1
	v_cvt_pk_bf16_f32 v1, v2, v3
	v_cvt_pk_bf16_f32 v2, v4, v5
	v_cvt_pk_bf16_f32 v3, v6, v7
	v_cvt_pk_bf16_f32 v4, v8, v9
	v_cvt_pk_bf16_f32 v5, v10, v11
	v_cvt_pk_bf16_f32 v6, v12, v13
	v_cvt_pk_bf16_f32 v7, v14, v15
	ds_write_b128 v82, v[0:3] offset:20480
	ds_write_b128 v82, v[4:7] offset:21504
	s_waitcnt lgkmcnt(0)
	s_barrier
	s_mov_b32 s5, m0
	s_mov_b32 m0, s23
	s_nop 0
	global_load_lds_dwordx4 v192, s[14:15]
	s_mov_b32 m0, s5
	s_nop 0
	s_mov_b32 s5, m0
	s_mov_b32 m0, s24
	s_nop 0
	global_load_lds_dwordx4 v192, s[6:7]
	s_mov_b32 m0, s5
	s_add_u32 s6, s14, 0xa000
	s_mov_b32 s5, m0
	s_mov_b32 m0, s25
	s_nop 0
	global_load_lds_dwordx4 v192, s[18:19]
	s_mov_b32 m0, s5
	s_addc_u32 s7, s15, 0
	s_mov_b32 s5, m0
	s_mov_b32 m0, s26
	s_nop 0
	global_load_lds_dwordx4 v192, s[34:35]
	s_mov_b32 m0, s5
	ds_read_b128 v[0:3], v80 offset:512
	ds_read2_b32 v[4:5], v80 offset0:136 offset1:137
	ds_read_b128 v[92:95], v100
	ds_read2_b32 v[6:7], v80 offset0:138 offset1:139
	ds_read2_b32 v[8:9], v80 offset0:144 offset1:145
	ds_read2_b32 v[10:11], v80 offset0:146 offset1:147
	ds_read2_b32 v[12:13], v80 offset0:152 offset1:153
	ds_read2_b32 v[14:15], v80 offset0:154 offset1:155
	ds_read_b128 v[96:99], v100 offset:256
	s_waitcnt lgkmcnt(1)
	v_mfma_f32_32x32x16_bf16 v[0:15], v[92:95], v[68:71], v[0:15]
	v_add_u32_e32 v100, v101, v102
	s_add_u32 s18, s14, 0xc000
	s_addc_u32 s19, s15, 0
	s_add_u32 s34, s14, 0xe000
	s_addc_u32 s35, s15, 0
	s_cmpk_gt_u32 s3, 0xff
	s_waitcnt lgkmcnt(0)
	v_mfma_f32_32x32x16_bf16 v[0:15], v[96:99], v[76:79], v[0:15]
	ds_read_b128 v[92:95], v100
	ds_read_b128 v[96:99], v100 offset:256
	v_add_u32_e32 v100, v101, v103
	s_waitcnt lgkmcnt(1)
	v_mfma_f32_32x32x16_bf16 v[0:15], v[92:95], v[60:63], v[0:15]
	s_waitcnt lgkmcnt(0)
	v_mfma_f32_32x32x16_bf16 v[0:15], v[96:99], v[72:75], v[0:15]
	ds_read_b128 v[92:95], v100
	ds_read_b128 v[96:99], v100 offset:256
	v_add_u32_e32 v100, v101, v104
	s_waitcnt lgkmcnt(1)
	v_mfma_f32_32x32x16_bf16 v[0:15], v[92:95], v[52:55], v[0:15]
	s_waitcnt lgkmcnt(0)
	v_mfma_f32_32x32x16_bf16 v[0:15], v[96:99], v[64:67], v[0:15]
	ds_read_b128 v[92:95], v100
	ds_read_b128 v[96:99], v100 offset:256
	v_add_u32_e32 v100, v101, v105
	s_waitcnt lgkmcnt(1)
	v_mfma_f32_32x32x16_bf16 v[0:15], v[92:95], v[48:51], v[0:15]
	s_waitcnt lgkmcnt(0)
	v_mfma_f32_32x32x16_bf16 v[0:15], v[96:99], v[56:59], v[0:15]
	ds_read_b128 v[92:95], v100
	ds_read_b128 v[96:99], v100 offset:256
	v_add_u32_e32 v100, v101, v106
	s_waitcnt lgkmcnt(1)
	v_mfma_f32_32x32x16_bf16 v[0:15], v[92:95], v[36:39], v[0:15]
	s_waitcnt lgkmcnt(0)
	v_mfma_f32_32x32x16_bf16 v[0:15], v[96:99], v[44:47], v[0:15]
	ds_read_b128 v[92:95], v100
	ds_read_b128 v[96:99], v100 offset:256
	s_waitcnt lgkmcnt(1)
	v_mfma_f32_32x32x16_bf16 v[0:15], v[92:95], v[28:31], v[0:15]
	s_waitcnt lgkmcnt(0)
	v_mfma_f32_32x32x16_bf16 v[0:15], v[96:99], v[40:43], v[0:15]
	ds_read_b128 v[92:95], v91
	ds_read_b128 v[96:99], v91 offset:256
	v_add_u32_e32 v91, v101, v107
	s_waitcnt lgkmcnt(1)
	v_mfma_f32_32x32x16_bf16 v[0:15], v[92:95], v[24:27], v[0:15]
	ds_read_b128 v[92:95], v91
	s_waitcnt lgkmcnt(1)
	v_mfma_f32_32x32x16_bf16 v[0:15], v[96:99], v[32:35], v[0:15]
	ds_read_b128 v[96:99], v91 offset:256
	ds_read_b128 v[144:147], v81 offset:20480
	ds_read_b128 v[148:151], v81 offset:21504
	ds_read_b128 v[152:155], v81 offset:22528
	ds_read_b128 v[156:159], v81 offset:23552
	s_waitcnt lgkmcnt(5)
	v_mfma_f32_32x32x16_bf16 v[0:15], v[92:95], v[20:23], v[0:15]
	s_waitcnt lgkmcnt(4)
	v_mfma_f32_32x32x16_bf16 v[0:15], v[96:99], v[16:19], v[0:15]
	s_nop 11
	v_cvt_pk_bf16_f32 v0, v0, v1
	v_cvt_pk_bf16_f32 v1, v2, v3
	v_cvt_pk_bf16_f32 v2, v4, v5
	v_cvt_pk_bf16_f32 v3, v6, v7
	v_cvt_pk_bf16_f32 v4, v8, v9
	v_cvt_pk_bf16_f32 v5, v10, v11
	v_cvt_pk_bf16_f32 v6, v12, v13
	v_cvt_pk_bf16_f32 v7, v14, v15
	ds_write_b128 v82, v[0:3]
	ds_write_b128 v82, v[4:7] offset:1024
	s_waitcnt vmcnt(4) lgkmcnt(0)
	s_barrier
	s_mov_b32 s5, m0
	s_mov_b32 m0, s27
	s_nop 0
	global_load_lds_dwordx4 v192, s[16:17]
	s_mov_b32 m0, s5
	s_nop 0
	s_mov_b32 s5, m0
	s_mov_b32 m0, s28
	s_nop 0
	global_load_lds_dwordx4 v192, s[6:7]
	s_mov_b32 m0, s5
	s_movk_i32 s7, 0x80
	s_mov_b32 s5, m0
	s_mov_b32 m0, s29
	s_nop 0
	global_load_lds_dwordx4 v192, s[18:19]
	s_mov_b32 m0, s5
	s_movk_i32 s6, 0xc0
	s_mov_b32 s5, m0
	s_mov_b32 m0, s30
	s_nop 0
	global_load_lds_dwordx4 v192, s[34:35]
	s_mov_b32 m0, s5
	ds_read_b128 v[0:3], v80 offset:768
	ds_read2_b32 v[4:5], v80 offset0:200 offset1:201
	ds_read_b128 v[92:95], v83
	ds_read2_b32 v[6:7], v80 offset0:202 offset1:203
	ds_read2_b32 v[8:9], v80 offset0:208 offset1:209
	ds_read2_b32 v[10:11], v80 offset0:210 offset1:211
	ds_read2_b32 v[12:13], v80 offset0:216 offset1:217
	ds_read2_b32 v[14:15], v80 offset0:218 offset1:219
	ds_read_b128 v[96:99], v83 offset:256
	s_waitcnt lgkmcnt(1)
	v_mfma_f32_32x32x16_bf16 v[0:15], v[92:95], v[68:71], v[0:15]
	s_mov_b32 s5, 0x10000
	s_waitcnt lgkmcnt(0)
	v_mfma_f32_32x32x16_bf16 v[0:15], v[96:99], v[76:79], v[0:15]
	ds_read_b128 v[68:71], v84
	ds_read_b128 v[76:79], v84 offset:256
	s_waitcnt lgkmcnt(1)
	v_mfma_f32_32x32x16_bf16 v[0:15], v[68:71], v[60:63], v[0:15]
	ds_read_b128 v[60:63], v85
	ds_read_b128 v[68:71], v85 offset:256
	s_waitcnt lgkmcnt(2)
	v_mfma_f32_32x32x16_bf16 v[0:15], v[76:79], v[72:75], v[0:15]
	s_waitcnt lgkmcnt(1)
	v_mfma_f32_32x32x16_bf16 v[0:15], v[60:63], v[52:55], v[0:15]
	ds_read_b128 v[52:55], v86
	ds_read_b128 v[60:63], v86 offset:256
	s_waitcnt lgkmcnt(2)
	v_mfma_f32_32x32x16_bf16 v[0:15], v[68:71], v[64:67], v[0:15]
	s_waitcnt lgkmcnt(1)
	v_mfma_f32_32x32x16_bf16 v[0:15], v[52:55], v[48:51], v[0:15]
	ds_read_b128 v[48:51], v87
	ds_read_b128 v[52:55], v87 offset:256
	s_waitcnt lgkmcnt(2)
	v_mfma_f32_32x32x16_bf16 v[0:15], v[60:63], v[56:59], v[0:15]
	s_waitcnt lgkmcnt(1)
	v_mfma_f32_32x32x16_bf16 v[0:15], v[48:51], v[36:39], v[0:15]
	s_waitcnt lgkmcnt(0)
	v_mfma_f32_32x32x16_bf16 v[0:15], v[52:55], v[44:47], v[0:15]
	ds_read_b128 v[36:39], v88
	ds_read_b128 v[44:47], v88 offset:256
	s_waitcnt lgkmcnt(1)
	v_mfma_f32_32x32x16_bf16 v[0:15], v[36:39], v[28:31], v[0:15]
	ds_read_b128 v[28:31], v90
	ds_read_b128 v[36:39], v90 offset:256
	s_waitcnt lgkmcnt(2)
	v_mfma_f32_32x32x16_bf16 v[0:15], v[44:47], v[40:43], v[0:15]
	s_waitcnt lgkmcnt(1)
	v_mfma_f32_32x32x16_bf16 v[0:15], v[28:31], v[24:27], v[0:15]
	ds_read_b128 v[24:27], v89
	ds_read_b128 v[28:31], v89 offset:256
	ds_read_b128 v[160:163], v81
	ds_read_b128 v[164:167], v81 offset:1024
	ds_read_b128 v[168:171], v81 offset:2048
	ds_read_b128 v[172:175], v81 offset:3072
	s_waitcnt lgkmcnt(6)
	v_mfma_f32_32x32x16_bf16 v[0:15], v[36:39], v[32:35], v[0:15]
	s_waitcnt lgkmcnt(5)
	v_mfma_f32_32x32x16_bf16 v[0:15], v[24:27], v[20:23], v[0:15]
	v_mbcnt_lo_u32_b32 v20, -1, 0
	v_mbcnt_hi_u32_b32 v193, -1, v20
	v_mov_b32_e32 v194, v193
	s_waitcnt lgkmcnt(4)
	v_mfma_f32_32x32x16_bf16 v[0:15], v[28:31], v[16:19], v[0:15]
	s_nop 11
	v_cvt_pk_bf16_f32 v0, v0, v1
	v_cvt_pk_bf16_f32 v1, v2, v3
	v_cvt_pk_bf16_f32 v2, v4, v5
	v_cvt_pk_bf16_f32 v3, v6, v7
	v_cvt_pk_bf16_f32 v4, v8, v9
	v_cvt_pk_bf16_f32 v5, v10, v11
	v_cvt_pk_bf16_f32 v6, v12, v13
	v_cvt_pk_bf16_f32 v7, v14, v15
	ds_write_b128 v82, v[0:3] offset:20480
	ds_write_b128 v82, v[4:7] offset:21504
	s_waitcnt vmcnt(4) lgkmcnt(0)
	s_barrier
	ds_read_b128 v[176:179], v81 offset:20480
	ds_read_b128 v[180:183], v81 offset:21504
	ds_read_b128 v[184:187], v81 offset:22528
	ds_read_b128 v[188:191], v81 offset:23552
	s_waitcnt lgkmcnt(0)
	s_barrier
	s_nop 0
	v_and_b32_e32 v196, 31, v194
	v_ashrrev_i32_e32 v197, 5, v194
	v_lshlrev_b32_e32 v195, 2, v194
	v_bfe_u32 v198, v194, 2, 2
	s_cbranch_scc0 .LBB1_16
	v_lshl_add_u32 v0, s20, 2, v197
	v_lshlrev_b32_e32 v3, 2, v197
	v_add_u32_e32 v1, 2, v0
	v_lshlrev_b32_e32 v2, 9, v0
	v_and_b32_e32 v3, 12, v3
	v_bfe_u32 v0, v0, 2, 2
	v_bitop3_b32 v0, v0, v196, v3 bitop3:0x36
	v_lshl_or_b32 v199, v0, 4, v2
	v_lshlrev_b32_e32 v0, 2, v1
	s_bfe_u32 s18, s3, 0x10006
	v_and_b32_e32 v0, 12, v0
	v_bfe_u32 v2, v1, 2, 2
	v_bitop3_b32 v0, v0, v196, v2 bitop3:0x36
	v_lshrrev_b32_e32 v2, 3, v194
	s_lshl_b32 s16, s18, 8
	v_and_b32_e32 v2, 2, v2
	v_bfe_u32 v3, v194, 1, 1
	s_add_i32 s16, s16, 0
	v_lshlrev_b32_e32 v4, 3, v194
	v_lshl_add_u32 v5, v197, 11, s16
	v_bitop3_b32 v2, v2, v197, v3 bitop3:0x36
	v_and_or_b32 v4, v4, 8, v5
	v_lshlrev_b32_e32 v2, 4, v2
	v_lshlrev_b32_e32 v3, 6, v198
	v_lshl_add_u32 v4, v198, 9, v4
	v_or_b32_e32 v5, v2, v3
	v_add_u32_e32 v200, v4, v5
	v_bitop3_b32 v5, v2, v3, 32 bitop3:0xde
	v_add_u32_e32 v6, 0x1000, v4
	v_add_u32_e32 v201, v6, v5
	v_xor_b32_e32 v5, 64, v3
	v_bitop3_b32 v5, v2, v5, 32 bitop3:0xde
	v_add_u32_e32 v203, v6, v5
	v_xor_b32_e32 v5, 0x80, v3
	v_bitop3_b32 v7, v2, v3, 64 bitop3:0xf6
	v_bitop3_b32 v5, v2, v5, 32 bitop3:0xde
	v_add_u32_e32 v202, v4, v7
	v_bitop3_b32 v7, v2, v3, s7 bitop3:0xf6
	v_add_u32_e32 v205, v6, v5
	v_xor_b32_e32 v5, 0xc0, v3
	v_bitop3_b32 v3, v2, v3, s6 bitop3:0xf6
	s_and_b32 s6, s22, 2
	v_lshlrev_b32_e32 v1, 9, v1
	s_lshl_b32 s27, s6, 2
	s_lshl_b32 s7, s6, 8
	s_lshl_b32 s6, s6, 12
	v_lshl_or_b32 v208, v0, 4, v1
	s_lshl_b32 s19, s20, 11
	s_add_i32 s7, s7, 0
	s_add_i32 s6, s6, 0
	v_mov_b32_e32 v0, 0
	v_bitop3_b32 v2, v2, v5, 32 bitop3:0xde
	s_waitcnt vmcnt(0)
	s_add_i32 s19, s19, 0
	s_add_i32 s16, s7, 0x20000
	s_add_i32 s7, s7, 0x20100
	v_lshlrev_b32_e32 v209, 4, v194
	s_add_i32 s6, s6, 0x18000
	v_mov_b32_e32 v14, v0
	v_mov_b32_e32 v15, v0
	v_add_u32_e32 v204, v4, v7
	v_add_u32_e32 v206, v4, v3
	v_add_u32_e32 v207, v6, v2
	v_add_u32_e32 v212, s6, v209
	s_add_u32 s6, s8, 0xfff90000
	v_mov_b32_e32 v1, v0
	v_mov_b32_e32 v2, v0
	v_mov_b32_e32 v3, v0
	v_mov_b32_e32 v4, v0
	v_mov_b32_e32 v5, v0
	v_mov_b32_e32 v6, v0
	v_mov_b32_e32 v7, v0
	v_mov_b32_e32 v8, v0
	v_mov_b32_e32 v9, v0
	v_mov_b32_e32 v10, v0
	v_mov_b32_e32 v11, v0
	v_mov_b32_e32 v12, v0
	v_mov_b32_e32 v13, v0
	v_mov_b64_e32 v[62:63], v[14:15]
	v_mov_b64_e32 v[94:95], v[14:15]
	v_mov_b64_e32 v[126:127], v[14:15]
	v_mov_b64_e32 v[30:31], v[14:15]
	v_mov_b64_e32 v[46:47], v[14:15]
	v_mov_b64_e32 v[78:79], v[14:15]
	v_mov_b64_e32 v[110:111], v[14:15]
	v_add_u32_e32 v210, s16, v195
	v_add_u32_e32 v211, s7, v195
	s_addc_u32 s7, s9, -1
	s_mov_b32 s33, 1
	s_mov_b32 s31, 0x8000
	s_mov_b32 s29, 0x10000
	v_mov_b64_e32 v[60:61], v[12:13]
	v_mov_b64_e32 v[58:59], v[10:11]
	v_mov_b64_e32 v[56:57], v[8:9]
	v_mov_b64_e32 v[54:55], v[6:7]
	v_mov_b64_e32 v[52:53], v[4:5]
	v_mov_b64_e32 v[50:51], v[2:3]
	v_mov_b64_e32 v[48:49], v[0:1]
	v_mov_b64_e32 v[92:93], v[12:13]
	v_mov_b64_e32 v[90:91], v[10:11]
	v_mov_b64_e32 v[88:89], v[8:9]
	v_mov_b64_e32 v[86:87], v[6:7]
	v_mov_b64_e32 v[84:85], v[4:5]
	v_mov_b64_e32 v[82:83], v[2:3]
	v_mov_b64_e32 v[80:81], v[0:1]
	v_mov_b64_e32 v[124:125], v[12:13]
	v_mov_b64_e32 v[122:123], v[10:11]
	v_mov_b64_e32 v[120:121], v[8:9]
	v_mov_b64_e32 v[118:119], v[6:7]
	v_mov_b64_e32 v[116:117], v[4:5]
	v_mov_b64_e32 v[114:115], v[2:3]
	v_mov_b64_e32 v[112:113], v[0:1]
	v_mov_b64_e32 v[28:29], v[12:13]
	v_mov_b64_e32 v[26:27], v[10:11]
	v_mov_b64_e32 v[24:25], v[8:9]
	v_mov_b64_e32 v[22:23], v[6:7]
	v_mov_b64_e32 v[20:21], v[4:5]
	v_mov_b64_e32 v[18:19], v[2:3]
	v_mov_b64_e32 v[16:17], v[0:1]
	v_mov_b64_e32 v[44:45], v[12:13]
	v_mov_b64_e32 v[42:43], v[10:11]
	v_mov_b64_e32 v[40:41], v[8:9]
	v_mov_b64_e32 v[38:39], v[6:7]
	v_mov_b64_e32 v[36:37], v[4:5]
	v_mov_b64_e32 v[34:35], v[2:3]
	v_mov_b64_e32 v[32:33], v[0:1]
	v_mov_b64_e32 v[76:77], v[12:13]
	v_mov_b64_e32 v[74:75], v[10:11]
	v_mov_b64_e32 v[72:73], v[8:9]
	v_mov_b64_e32 v[70:71], v[6:7]
	v_mov_b64_e32 v[68:69], v[4:5]
	v_mov_b64_e32 v[66:67], v[2:3]
	v_mov_b64_e32 v[64:65], v[0:1]
	v_mov_b64_e32 v[108:109], v[12:13]
	v_mov_b64_e32 v[106:107], v[10:11]
	v_mov_b64_e32 v[104:105], v[8:9]
	v_mov_b64_e32 v[102:103], v[6:7]
	v_mov_b64_e32 v[100:101], v[4:5]
	v_mov_b64_e32 v[98:99], v[2:3]
	v_mov_b64_e32 v[96:97], v[0:1]
	s_waitcnt lgkmcnt(0)
	v_mov_b64_e32 v[128:129], v[14:15]
	v_mov_b64_e32 v[130:131], v[14:15]
	v_mov_b64_e32 v[132:133], v[14:15]
	v_mov_b64_e32 v[134:135], v[14:15]
	v_mov_b64_e32 v[136:137], v[14:15]
	v_mov_b64_e32 v[138:139], v[14:15]
	v_mov_b64_e32 v[140:141], v[14:15]
	v_mov_b64_e32 v[142:143], v[14:15]
	v_mov_b64_e32 v[144:145], v[14:15]
	v_mov_b64_e32 v[146:147], v[14:15]
	v_mov_b64_e32 v[148:149], v[14:15]
	v_mov_b64_e32 v[150:151], v[14:15]
	v_add_u32_e32 v238, s31, v200
	v_add_u32_e32 v239, s31, v201
	v_add_u32_e32 v240, s31, v202
	v_add_u32_e32 v241, s31, v203
	v_add_u32_e32 v242, s31, v204
	v_add_u32_e32 v243, s31, v205
	v_add_u32_e32 v244, s31, v206
	v_add_u32_e32 v245, s31, v207
	ds_read_b64_tr_b16 v[222:223], v238 offset:0
	ds_read_b64_tr_b16 v[224:225], v239 offset:0
	ds_read_b64_tr_b16 v[226:227], v240 offset:0
	ds_read_b64_tr_b16 v[228:229], v241 offset:0
	ds_read_b64_tr_b16 v[230:231], v242 offset:0
	ds_read_b64_tr_b16 v[232:233], v243 offset:0
	ds_read_b64_tr_b16 v[234:235], v244 offset:0
	ds_read_b64_tr_b16 v[236:237], v245 offset:0
	s_barrier

.LBB1_10:
	s_add_i32 s29, s28, 0x8000
	s_cmp_lg_u32 s28, 0x10000
	s_cselect_b32 s29, s29, 0
	s_add_i32 s36, s19, s29
	s_andn2_b32 s38, 1, s33
	s_lshl_b32 s34, s38, 4
	s_add_i32 s34, s34, s27
	s_add_i32 s34, s34, 0x20800
	v_mov_b32_e32 v154, s34
	v_lshl_add_u32 v213, s38, 14, v212
	ds_read_b64 v[154:155], v154
	ds_read_b128 v[214:217], v213
	ds_read_b128 v[218:221], v213 offset:4096
	s_mov_b32 m0, s36
	v_mfma_f32_32x32x16_bf16 v[112:127], v[136:139], v[128:131], v[112:127]
	global_load_lds_dwordx4 v199, s[16:17]
	s_add_i32 s34, s36, 0x400
	s_mov_b32 m0, s34
	v_mfma_f32_32x32x16_bf16 v[96:111], v[136:139], v[132:135], v[96:111]
	global_load_lds_dwordx4 v208, s[16:17]
	s_add_u32 s34, s16, 0x2000
	s_addc_u32 s35, s17, 0
	s_add_i32 s37, s36, 0x2000
	s_mov_b32 m0, s37
	v_mfma_f32_32x32x16_bf16 v[80:95], v[140:143], v[128:131], v[80:95]
	global_load_lds_dwordx4 v199, s[34:35]
	s_add_i32 s37, s36, 0x2400
	s_mov_b32 m0, s37
	v_mfma_f32_32x32x16_bf16 v[64:79], v[140:143], v[132:135], v[64:79]
	global_load_lds_dwordx4 v208, s[34:35]
	s_add_u32 s34, s16, 0x4000
	s_addc_u32 s35, s17, 0
	s_add_i32 s37, s36, 0x4000
	s_mov_b32 m0, s37
	v_mfma_f32_32x32x16_bf16 v[48:63], v[144:147], v[128:131], v[48:63]
	global_load_lds_dwordx4 v199, s[34:35]
	s_add_i32 s37, s36, 0x4400
	s_mov_b32 m0, s37
	v_mfma_f32_32x32x16_bf16 v[32:47], v[144:147], v[132:135], v[32:47]
	global_load_lds_dwordx4 v208, s[34:35]
	s_add_u32 s34, s16, 0x6000
	s_addc_u32 s35, s17, 0
	s_add_i32 s37, s36, 0x6000
	s_mov_b32 m0, s37
	v_mfma_f32_32x32x16_bf16 v[0:15], v[148:151], v[128:131], v[0:15]
	global_load_lds_dwordx4 v199, s[34:35]
	s_add_i32 s37, s36, 0x6400
	s_mov_b32 m0, s37
	v_mfma_f32_32x32x16_bf16 v[16:31], v[148:151], v[132:135], v[16:31]
	global_load_lds_dwordx4 v208, s[34:35]
	s_add_u32 s6, s6, 0x8000
	s_addc_u32 s7, s7, 0
	s_waitcnt lgkmcnt(2)
	v_readfirstlane_b32 s34, v154
	v_readfirstlane_b32 s35, v155
	s_cmp_eq_u32 s34, 0
	s_cbranch_scc1 .Lpv_noA
	v_lshl_add_u32 v152, s38, 10, v210
	ds_read_b32 v152, v152
	s_nop 7
	s_waitcnt lgkmcnt(0)
	v_pk_mul_f32 v[126:127], v[152:153], v[126:127] op_sel_hi:[0,1]
	v_pk_mul_f32 v[124:125], v[152:153], v[124:125] op_sel_hi:[0,1]
	v_pk_mul_f32 v[122:123], v[152:153], v[122:123] op_sel_hi:[0,1]
	v_pk_mul_f32 v[120:121], v[152:153], v[120:121] op_sel_hi:[0,1]
	v_pk_mul_f32 v[118:119], v[152:153], v[118:119] op_sel_hi:[0,1]
	v_pk_mul_f32 v[116:117], v[152:153], v[116:117] op_sel_hi:[0,1]
	v_pk_mul_f32 v[114:115], v[152:153], v[114:115] op_sel_hi:[0,1]
	v_pk_mul_f32 v[112:113], v[152:153], v[112:113] op_sel_hi:[0,1]
	v_pk_mul_f32 v[94:95], v[152:153], v[94:95] op_sel_hi:[0,1]
	v_pk_mul_f32 v[92:93], v[152:153], v[92:93] op_sel_hi:[0,1]
	v_pk_mul_f32 v[90:91], v[152:153], v[90:91] op_sel_hi:[0,1]
	v_pk_mul_f32 v[88:89], v[152:153], v[88:89] op_sel_hi:[0,1]
	v_pk_mul_f32 v[86:87], v[152:153], v[86:87] op_sel_hi:[0,1]
	v_pk_mul_f32 v[84:85], v[152:153], v[84:85] op_sel_hi:[0,1]
	v_pk_mul_f32 v[82:83], v[152:153], v[82:83] op_sel_hi:[0,1]
	v_pk_mul_f32 v[80:81], v[152:153], v[80:81] op_sel_hi:[0,1]
	v_pk_mul_f32 v[62:63], v[152:153], v[62:63] op_sel_hi:[0,1]
	v_pk_mul_f32 v[60:61], v[152:153], v[60:61] op_sel_hi:[0,1]
	v_pk_mul_f32 v[58:59], v[152:153], v[58:59] op_sel_hi:[0,1]
	v_pk_mul_f32 v[56:57], v[152:153], v[56:57] op_sel_hi:[0,1]
	v_pk_mul_f32 v[54:55], v[152:153], v[54:55] op_sel_hi:[0,1]
	v_pk_mul_f32 v[52:53], v[152:153], v[52:53] op_sel_hi:[0,1]
	v_pk_mul_f32 v[50:51], v[152:153], v[50:51] op_sel_hi:[0,1]
	v_pk_mul_f32 v[48:49], v[152:153], v[48:49] op_sel_hi:[0,1]
	v_pk_mul_f32 v[14:15], v[152:153], v[14:15] op_sel_hi:[0,1]
	v_pk_mul_f32 v[12:13], v[152:153], v[12:13] op_sel_hi:[0,1]
	v_pk_mul_f32 v[10:11], v[152:153], v[10:11] op_sel_hi:[0,1]
	v_pk_mul_f32 v[8:9], v[152:153], v[8:9] op_sel_hi:[0,1]
	v_pk_mul_f32 v[6:7], v[152:153], v[6:7] op_sel_hi:[0,1]
	v_pk_mul_f32 v[4:5], v[152:153], v[4:5] op_sel_hi:[0,1]
	v_pk_mul_f32 v[2:3], v[152:153], v[2:3] op_sel_hi:[0,1]
	v_pk_mul_f32 v[0:1], v[152:153], v[0:1] op_sel_hi:[0,1]
.Lpv_noA:
	s_cmp_eq_u32 s35, 0
	s_cbranch_scc1 .Lpv_noB
	v_lshl_add_u32 v152, s38, 10, v211
	ds_read_b32 v152, v152
	s_nop 7
	s_waitcnt lgkmcnt(0)
	v_pk_mul_f32 v[110:111], v[152:153], v[110:111] op_sel_hi:[0,1]
	v_pk_mul_f32 v[108:109], v[152:153], v[108:109] op_sel_hi:[0,1]
	v_pk_mul_f32 v[106:107], v[152:153], v[106:107] op_sel_hi:[0,1]
	v_pk_mul_f32 v[104:105], v[152:153], v[104:105] op_sel_hi:[0,1]
	v_pk_mul_f32 v[102:103], v[152:153], v[102:103] op_sel_hi:[0,1]
	v_pk_mul_f32 v[100:101], v[152:153], v[100:101] op_sel_hi:[0,1]
	v_pk_mul_f32 v[98:99], v[152:153], v[98:99] op_sel_hi:[0,1]
	v_pk_mul_f32 v[96:97], v[152:153], v[96:97] op_sel_hi:[0,1]
	v_pk_mul_f32 v[78:79], v[152:153], v[78:79] op_sel_hi:[0,1]
	v_pk_mul_f32 v[76:77], v[152:153], v[76:77] op_sel_hi:[0,1]
	v_pk_mul_f32 v[74:75], v[152:153], v[74:75] op_sel_hi:[0,1]
	v_pk_mul_f32 v[72:73], v[152:153], v[72:73] op_sel_hi:[0,1]
	v_pk_mul_f32 v[70:71], v[152:153], v[70:71] op_sel_hi:[0,1]
	v_pk_mul_f32 v[68:69], v[152:153], v[68:69] op_sel_hi:[0,1]
	v_pk_mul_f32 v[66:67], v[152:153], v[66:67] op_sel_hi:[0,1]
	v_pk_mul_f32 v[64:65], v[152:153], v[64:65] op_sel_hi:[0,1]
	v_pk_mul_f32 v[46:47], v[152:153], v[46:47] op_sel_hi:[0,1]
	v_pk_mul_f32 v[44:45], v[152:153], v[44:45] op_sel_hi:[0,1]
	v_pk_mul_f32 v[42:43], v[152:153], v[42:43] op_sel_hi:[0,1]
	v_pk_mul_f32 v[40:41], v[152:153], v[40:41] op_sel_hi:[0,1]
	v_pk_mul_f32 v[38:39], v[152:153], v[38:39] op_sel_hi:[0,1]
	v_pk_mul_f32 v[36:37], v[152:153], v[36:37] op_sel_hi:[0,1]
	v_pk_mul_f32 v[34:35], v[152:153], v[34:35] op_sel_hi:[0,1]
	v_pk_mul_f32 v[32:33], v[152:153], v[32:33] op_sel_hi:[0,1]
	v_pk_mul_f32 v[30:31], v[152:153], v[30:31] op_sel_hi:[0,1]
	v_pk_mul_f32 v[28:29], v[152:153], v[28:29] op_sel_hi:[0,1]
	v_pk_mul_f32 v[26:27], v[152:153], v[26:27] op_sel_hi:[0,1]
	v_pk_mul_f32 v[24:25], v[152:153], v[24:25] op_sel_hi:[0,1]
	v_pk_mul_f32 v[22:23], v[152:153], v[22:23] op_sel_hi:[0,1]
	v_pk_mul_f32 v[20:21], v[152:153], v[20:21] op_sel_hi:[0,1]
	v_pk_mul_f32 v[18:19], v[152:153], v[18:19] op_sel_hi:[0,1]
	v_pk_mul_f32 v[16:17], v[152:153], v[16:17] op_sel_hi:[0,1]
.Lpv_noB:
	s_waitcnt lgkmcnt(0)
	v_mfma_f32_32x32x16_bf16 v[112:127], v[222:225], v[214:217], v[112:127]
	ds_read_b128 v[128:131], v213 offset:1024
	ds_read_b64_tr_b16 v[136:137], v238 offset:8192
	ds_read_b64_tr_b16 v[138:139], v239 offset:8192
	v_mfma_f32_32x32x16_bf16 v[96:111], v[222:225], v[218:221], v[96:111]
	ds_read_b128 v[132:135], v213 offset:5120
	ds_read_b64_tr_b16 v[140:141], v240 offset:8192
	ds_read_b64_tr_b16 v[142:143], v241 offset:8192
	v_mfma_f32_32x32x16_bf16 v[80:95], v[226:229], v[214:217], v[80:95]
	ds_read_b64_tr_b16 v[144:145], v242 offset:8192
	ds_read_b64_tr_b16 v[146:147], v243 offset:8192
	v_mfma_f32_32x32x16_bf16 v[64:79], v[226:229], v[218:221], v[64:79]
	ds_read_b64_tr_b16 v[148:149], v244 offset:8192
	ds_read_b64_tr_b16 v[150:151], v245 offset:8192
	v_mfma_f32_32x32x16_bf16 v[48:63], v[230:233], v[214:217], v[48:63]
	v_mfma_f32_32x32x16_bf16 v[32:47], v[230:233], v[218:221], v[32:47]
	v_mfma_f32_32x32x16_bf16 v[0:15], v[234:237], v[214:217], v[0:15]
	v_mfma_f32_32x32x16_bf16 v[16:31], v[234:237], v[218:221], v[16:31]
	s_waitcnt lgkmcnt(0)
	v_mfma_f32_32x32x16_bf16 v[112:127], v[136:139], v[128:131], v[112:127]
	ds_read_b128 v[214:217], v213 offset:2048
	ds_read_b64_tr_b16 v[222:223], v238 offset:16384
	ds_read_b64_tr_b16 v[224:225], v239 offset:16384
	v_mfma_f32_32x32x16_bf16 v[96:111], v[136:139], v[132:135], v[96:111]
	ds_read_b128 v[218:221], v213 offset:6144
	ds_read_b64_tr_b16 v[226:227], v240 offset:16384
	ds_read_b64_tr_b16 v[228:229], v241 offset:16384
	v_mfma_f32_32x32x16_bf16 v[80:95], v[140:143], v[128:131], v[80:95]
	ds_read_b64_tr_b16 v[230:231], v242 offset:16384
	ds_read_b64_tr_b16 v[232:233], v243 offset:16384
	v_mfma_f32_32x32x16_bf16 v[64:79], v[140:143], v[132:135], v[64:79]
	ds_read_b64_tr_b16 v[234:235], v244 offset:16384
	ds_read_b64_tr_b16 v[236:237], v245 offset:16384
	v_mfma_f32_32x32x16_bf16 v[48:63], v[144:147], v[128:131], v[48:63]
	v_mfma_f32_32x32x16_bf16 v[32:47], v[144:147], v[132:135], v[32:47]
	v_mfma_f32_32x32x16_bf16 v[0:15], v[148:151], v[128:131], v[0:15]
	v_mfma_f32_32x32x16_bf16 v[16:31], v[148:151], v[132:135], v[16:31]
	s_waitcnt lgkmcnt(0)
	v_mfma_f32_32x32x16_bf16 v[112:127], v[222:225], v[214:217], v[112:127]
	ds_read_b128 v[128:131], v213 offset:3072
	ds_read_b64_tr_b16 v[136:137], v238 offset:24576
	ds_read_b64_tr_b16 v[138:139], v239 offset:24576
	v_mfma_f32_32x32x16_bf16 v[96:111], v[222:225], v[218:221], v[96:111]
	ds_read_b128 v[132:135], v213 offset:7168
	ds_read_b64_tr_b16 v[140:141], v240 offset:24576
	ds_read_b64_tr_b16 v[142:143], v241 offset:24576
	v_mfma_f32_32x32x16_bf16 v[80:95], v[226:229], v[214:217], v[80:95]
	ds_read_b64_tr_b16 v[144:145], v242 offset:24576
	ds_read_b64_tr_b16 v[146:147], v243 offset:24576
	v_mfma_f32_32x32x16_bf16 v[64:79], v[226:229], v[218:221], v[64:79]
	ds_read_b64_tr_b16 v[148:149], v244 offset:24576
	ds_read_b64_tr_b16 v[150:151], v245 offset:24576
	v_mfma_f32_32x32x16_bf16 v[48:63], v[230:233], v[214:217], v[48:63]
	v_mfma_f32_32x32x16_bf16 v[32:47], v[230:233], v[218:221], v[32:47]
	v_mfma_f32_32x32x16_bf16 v[0:15], v[234:237], v[214:217], v[0:15]
	v_mfma_f32_32x32x16_bf16 v[16:31], v[234:237], v[218:221], v[16:31]
	s_waitcnt lgkmcnt(0)
	v_add_u32_e32 v238, s28, v200
	v_add_u32_e32 v239, s28, v201
	v_add_u32_e32 v240, s28, v202
	v_add_u32_e32 v241, s28, v203
	v_add_u32_e32 v242, s28, v204
	v_add_u32_e32 v243, s28, v205
	v_add_u32_e32 v244, s28, v206
	v_add_u32_e32 v245, s28, v207
	ds_read_b64_tr_b16 v[222:223], v238 offset:0
	ds_read_b64_tr_b16 v[224:225], v239 offset:0
	ds_read_b64_tr_b16 v[226:227], v240 offset:0
	ds_read_b64_tr_b16 v[228:229], v241 offset:0
	ds_read_b64_tr_b16 v[230:231], v242 offset:0
	ds_read_b64_tr_b16 v[232:233], v243 offset:0
	ds_read_b64_tr_b16 v[234:235], v244 offset:0
	ds_read_b64_tr_b16 v[236:237], v245 offset:0
	s_waitcnt vmcnt(0)
	s_barrier
	s_cmp_eq_u32 s30, 17
	s_cbranch_scc1 .Lpv_exit
	s_mov_b32 s33, s30
	s_branch .LBB1_8
.Lpv_exit:
	v_mfma_f32_32x32x16_bf16 v[112:127], v[136:139], v[128:131], v[112:127]
	v_mfma_f32_32x32x16_bf16 v[96:111], v[136:139], v[132:135], v[96:111]
	v_mfma_f32_32x32x16_bf16 v[80:95], v[140:143], v[128:131], v[80:95]
	v_mfma_f32_32x32x16_bf16 v[64:79], v[140:143], v[132:135], v[64:79]
	v_mfma_f32_32x32x16_bf16 v[48:63], v[144:147], v[128:131], v[48:63]
	v_mfma_f32_32x32x16_bf16 v[32:47], v[144:147], v[132:135], v[32:47]
	v_mfma_f32_32x32x16_bf16 v[0:15], v[148:151], v[128:131], v[0:15]
	v_mfma_f32_32x32x16_bf16 v[16:31], v[148:151], v[132:135], v[16:31]
	s_nop 1
	s_branch .LBB1_17

.LBB1_18:
	s_lshl_b64 s[6:7], s[10:11], 20
	s_add_u32 s3, s12, s6
	s_addc_u32 s5, s13, s7
	s_lshl_b32 s10, s2, 2
	v_lshlrev_b32_e32 v0, 7, v194
	s_add_u32 s10, s3, s10
	v_and_b32_e32 v0, 0xfffffc00, v0
	s_addc_u32 s11, s5, 0
	v_ashrrev_i32_e32 v1, 31, v0
	v_lshl_add_u64 v[2:3], v[0:1], 2, s[10:11]
	v_and_b32_e32 v0, 28, v195
	v_lshlrev_b32_e32 v0, 2, v0
	v_mov_b32_e32 v1, 0
	v_lshl_add_u64 v[96:97], v[2:3], 0, v[0:1]
	s_mov_b32 s3, 0x8000
	v_add_co_u32_e32 v2, vcc, s3, v96
	s_waitcnt vmcnt(0)
	s_mov_b32 s5, 0x10000
	s_nop 0
	v_addc_co_u32_e32 v3, vcc, 0, v97, vcc
	global_load_dwordx4 v[52:55], v[96:97], off nt
	global_load_dwordx4 v[60:63], v[2:3], off nt
	v_add_co_u32_e32 v2, vcc, s5, v96
	s_mov_b32 s3, 0x18000
	s_nop 0
	v_addc_co_u32_e32 v3, vcc, 0, v97, vcc
	v_add_co_u32_e32 v4, vcc, s3, v96
	s_mov_b32 s3, 0x40000
	s_nop 0
	v_addc_co_u32_e32 v5, vcc, 0, v97, vcc
	global_load_dwordx4 v[76:79], v[2:3], off nt
	global_load_dwordx4 v[64:67], v[4:5], off nt
	v_add_co_u32_e32 v2, vcc, s3, v96
	s_mov_b32 s3, 0x48000
	s_nop 0
	v_addc_co_u32_e32 v3, vcc, 0, v97, vcc
	v_add_co_u32_e32 v4, vcc, s3, v96
	s_mov_b32 s3, 0x50000
	s_nop 0
	v_addc_co_u32_e32 v5, vcc, 0, v97, vcc
	global_load_dwordx4 v[68:71], v[2:3], off nt
	global_load_dwordx4 v[72:75], v[4:5], off nt
	v_add_co_u32_e32 v2, vcc, s3, v96
	s_mov_b32 s3, 0x58000
	s_nop 0
	v_addc_co_u32_e32 v3, vcc, 0, v97, vcc
	v_add_co_u32_e32 v4, vcc, s3, v96
	v_and_b32_e32 v0, 12, v195
	s_nop 0
	v_addc_co_u32_e32 v5, vcc, 0, v97, vcc
	global_load_dwordx4 v[56:59], v[2:3], off nt
	global_load_dwordx4 v[48:51], v[4:5], off nt
	v_bitop3_b32 v0, v0, v197, v198 bitop3:0x36
	v_lshlrev_b32_e32 v0, 4, v0
	v_lshl_add_u32 v2, v196, 9, 0
	s_movk_i32 s10, 0x60
	s_waitcnt vmcnt(13)
	v_xad_u32 v83, v0, s10, v2
	s_movk_i32 s10, 0x80
	s_waitcnt vmcnt(12)
	v_xad_u32 v84, v0, s10, v2
	s_movk_i32 s10, 0xa0
	v_xad_u32 v85, v0, s10, v2
	s_movk_i32 s10, 0xc0
	v_xad_u32 v86, v0, s10, v2
	s_movk_i32 s10, 0xe0
	v_xad_u32 v87, v0, s10, v2
	s_lshl_b32 s10, s22, 8
	s_add_i32 s10, s10, 0
	s_lshl_b32 s11, s22, 12
	v_add_u32_e32 v98, s10, v195
	s_lshl_b32 s10, s22, 2
	s_add_i32 s11, s11, 0
	v_add_u32_e32 v80, v2, v0
	v_xad_u32 v81, v0, 32, v2
	v_xad_u32 v82, v0, 64, v2
	s_add_i32 s10, s10, 0
	v_lshl_add_u32 v0, v194, 4, s11
	s_mov_b32 s3, 0
	v_add_u32_e32 v88, 0x20000, v98
	s_add_i32 s10, s10, 0x20800
	v_add_u32_e32 v89, 0x18000, v0
	s_setprio 1
	v_add_u32_e32 v0, 0x8000, v80
	ds_read_b128 v[2:5], v0
	ds_read_b128 v[18:21], v0 offset:256
	ds_read_b128 v[22:25], v0 offset:16384
	s_waitcnt vmcnt(8)
	ds_read_b128 v[34:37], v0 offset:16640
	v_add_u32_e32 v0, 0x8000, v81
	ds_read_b128 v[26:29], v0
	ds_read_b128 v[30:33], v0 offset:256
	ds_read_b128 v[38:41], v0 offset:16384
	ds_read_b128 v[42:45], v0 offset:16640
	s_waitcnt lgkmcnt(4)
	v_add_u32_e32 v0, 0x8000, v82
	v_mfma_f32_32x32x16_bf16 v[2:17], v[2:5], v[128:131], 0
	s_waitcnt lgkmcnt(0)
	v_mfma_f32_32x32x16_bf16 v[2:17], v[18:21], v[160:163], v[2:17]
	ds_read_b128 v[18:21], v0
	ds_read_b128 v[90:93], v0 offset:256
	ds_read_b128 v[100:103], v0 offset:16384
	ds_read_b128 v[104:107], v0 offset:16640
	s_waitcnt lgkmcnt(4)
	v_add_u32_e32 v0, 0x8000, v83
	v_mfma_f32_32x32x16_bf16 v[2:17], v[26:29], v[132:135], v[2:17]
	ds_read_b128 v[26:29], v0
	v_mfma_f32_32x32x16_bf16 v[2:17], v[30:33], v[164:167], v[2:17]
	ds_read_b128 v[30:33], v0 offset:256
	ds_read_b128 v[108:111], v0 offset:16384
	ds_read_b128 v[112:115], v0 offset:16640
	s_waitcnt lgkmcnt(4)
	v_add_u32_e32 v0, 0x8000, v84
	v_mfma_f32_32x32x16_bf16 v[2:17], v[18:21], v[136:139], v[2:17]
	ds_read_b128 v[18:21], v0
	v_mfma_f32_32x32x16_bf16 v[2:17], v[90:93], v[168:171], v[2:17]
	ds_read_b128 v[90:93], v0 offset:256
	ds_read_b128 v[116:119], v0 offset:16384
	ds_read_b128 v[120:123], v0 offset:16640
	s_waitcnt lgkmcnt(4)
	v_add_u32_e32 v0, 0x8000, v85
	v_mfma_f32_32x32x16_bf16 v[2:17], v[26:29], v[140:143], v[2:17]
	ds_read_b128 v[26:29], v0
	v_mfma_f32_32x32x16_bf16 v[2:17], v[30:33], v[172:175], v[2:17]
	ds_read_b128 v[30:33], v0 offset:256
	ds_read_b128 v[124:127], v0 offset:16384
	ds_read_b128 v[194:197], v0 offset:16640
	s_waitcnt lgkmcnt(4)
	v_add_u32_e32 v0, 0x8000, v86
	v_mfma_f32_32x32x16_bf16 v[2:17], v[18:21], v[144:147], v[2:17]
	ds_read_b128 v[18:21], v0
	v_mfma_f32_32x32x16_bf16 v[2:17], v[90:93], v[176:179], v[2:17]
	ds_read_b128 v[90:93], v0 offset:256
	ds_read_b128 v[198:201], v0 offset:16384
	ds_read_b128 v[202:205], v0 offset:16640
	s_waitcnt lgkmcnt(4)
	v_add_u32_e32 v0, 0x8000, v87
	v_mfma_f32_32x32x16_bf16 v[2:17], v[26:29], v[148:151], v[2:17]
	ds_read_b128 v[26:29], v0
	v_mfma_f32_32x32x16_bf16 v[2:17], v[30:33], v[180:183], v[2:17]
	ds_read_b128 v[30:33], v0 offset:256
	ds_read_b128 v[206:209], v0 offset:16384
	ds_read_b128 v[210:213], v0 offset:16640
	s_waitcnt lgkmcnt(4)
	s_nop 0
	s_waitcnt lgkmcnt(0)
	v_mfma_f32_32x32x16_bf16 v[2:17], v[18:21], v[152:155], v[2:17]
	v_mfma_f32_32x32x16_bf16 v[2:17], v[90:93], v[184:187], v[2:17]
	v_mfma_f32_32x32x16_bf16 v[2:17], v[26:29], v[156:159], v[2:17]
	v_mfma_f32_32x32x16_bf16 v[2:17], v[30:33], v[188:191], v[2:17]
	v_mfma_f32_32x32x16_bf16 v[18:33], v[22:25], v[128:131], 0
	s_nop 10
	v_max_f32_e32 v0, v3, v3
	ds_write_b32 v88, v1
	v_mov_b32_e32 v1, 1
	s_mov_b32 s11, 1
	s_mov_b32 s12, 0x41300000
	v_mfma_f32_32x32x16_bf16 v[18:33], v[34:37], v[160:163], v[18:33]
	v_max_f32_e32 v34, v2, v2
	v_max_f32_e32 v0, v34, v0
	v_max3_f32 v0, v0, v4, v5
	v_max3_f32 v0, v0, v6, v7
	v_max3_f32 v0, v0, v8, v9
	v_max3_f32 v0, v0, v10, v11
	v_max3_f32 v0, v0, v12, v13
	v_mfma_f32_32x32x16_bf16 v[18:33], v[38:41], v[132:135], v[18:33]
	v_max3_f32 v0, v0, v14, v15
	v_max3_f32 v0, v0, v16, v17
	v_mov_b32_e32 v34, s10
	ds_write_b32 v34, v1
	v_mfma_f32_32x32x16_bf16 v[18:33], v[42:45], v[164:167], v[18:33]
	v_mfma_f32_32x32x16_bf16 v[18:33], v[100:103], v[136:139], v[18:33]
	v_mfma_f32_32x32x16_bf16 v[18:33], v[104:107], v[168:171], v[18:33]
	v_mfma_f32_32x32x16_bf16 v[18:33], v[108:111], v[140:143], v[18:33]
	v_mfma_f32_32x32x16_bf16 v[18:33], v[112:115], v[172:175], v[18:33]
	v_mfma_f32_32x32x16_bf16 v[18:33], v[116:119], v[144:147], v[18:33]
	v_mfma_f32_32x32x16_bf16 v[18:33], v[120:123], v[176:179], v[18:33]
	v_mfma_f32_32x32x16_bf16 v[18:33], v[124:127], v[148:151], v[18:33]
	v_mfma_f32_32x32x16_bf16 v[18:33], v[194:197], v[180:183], v[18:33]
	v_mfma_f32_32x32x16_bf16 v[18:33], v[198:201], v[152:155], v[18:33]
	v_mfma_f32_32x32x16_bf16 v[18:33], v[202:205], v[184:187], v[18:33]
	v_mfma_f32_32x32x16_bf16 v[18:33], v[206:209], v[156:159], v[18:33]
	v_mfma_f32_32x32x16_bf16 v[18:33], v[210:213], v[188:191], v[18:33]
	s_setprio 0
	s_nop 10
	v_max3_f32 v0, v0, v18, v19
	v_max3_f32 v0, v0, v20, v21
	v_max3_f32 v0, v0, v22, v23
	v_max3_f32 v0, v0, v24, v25
	v_max3_f32 v0, v0, v26, v27
	v_max3_f32 v0, v0, v28, v29
	v_max3_f32 v0, v0, v30, v31
	v_max3_f32 v0, v0, v32, v33
	v_mov_b32_e32 v1, v0
	s_nop 1
	v_permlane32_swap_b32_e32 v0, v1
	v_max_f32_e32 v1, v1, v1
	v_max_f32_e32 v0, v0, v0
	v_max_f32_e32 v0, v0, v1
	v_add_f32_e32 v90, 0, v0
	v_add_f32_e64 v2, -v90, v2
	v_add_f32_e64 v3, -v90, v3
	v_add_f32_e64 v4, -v90, v4
	v_add_f32_e64 v5, -v90, v5
	v_add_f32_e64 v6, -v90, v6
	v_add_f32_e64 v7, -v90, v7
	v_add_f32_e64 v8, -v90, v8
	v_add_f32_e64 v9, -v90, v9
	v_add_f32_e64 v1, -v90, v18
	v_add_f32_e64 v18, -v90, v19
	v_add_f32_e64 v19, -v90, v20
	v_add_f32_e64 v20, -v90, v21
	v_add_f32_e64 v21, -v90, v22
	v_add_f32_e64 v22, -v90, v23
	v_add_f32_e64 v23, -v90, v24
	v_add_f32_e64 v24, -v90, v25
	v_add_f32_e64 v25, -v90, v26
	v_add_f32_e64 v26, -v90, v27
	v_add_f32_e64 v27, -v90, v28
	v_add_f32_e64 v28, -v90, v29
	v_add_f32_e64 v29, -v90, v30
	v_add_f32_e64 v30, -v90, v31
	v_add_f32_e64 v31, -v90, v32
	v_add_f32_e64 v32, -v90, v33
	v_add_f32_e64 v10, -v90, v10
	v_add_f32_e64 v11, -v90, v11
	v_add_f32_e64 v12, -v90, v12
	v_add_f32_e64 v13, -v90, v13
	v_add_f32_e64 v14, -v90, v14
	v_add_f32_e64 v15, -v90, v15
	v_add_f32_e64 v16, -v90, v16
	v_add_f32_e64 v17, -v90, v17
	v_exp_f32_e32 v33, v2
	v_exp_f32_e32 v34, v3
	v_exp_f32_e32 v35, v4
	v_exp_f32_e32 v36, v5
	v_exp_f32_e32 v37, v6
	v_exp_f32_e32 v38, v7
	v_exp_f32_e32 v39, v8
	v_exp_f32_e32 v40, v9
	v_exp_f32_e32 v41, v10
	v_exp_f32_e32 v42, v11
	v_exp_f32_e32 v43, v12
	v_exp_f32_e32 v44, v13
	v_exp_f32_e32 v45, v14
	v_exp_f32_e32 v46, v15
	v_exp_f32_e32 v47, v16
	v_exp_f32_e32 v91, v17
	v_exp_f32_e32 v92, v1
	v_exp_f32_e32 v93, v18
	v_exp_f32_e32 v94, v19
	v_exp_f32_e32 v95, v20
	v_exp_f32_e32 v99, v21
	v_exp_f32_e32 v100, v22
	v_exp_f32_e32 v101, v23
	v_exp_f32_e32 v102, v24
	v_exp_f32_e32 v103, v25
	v_exp_f32_e32 v104, v26
	v_exp_f32_e32 v105, v27
	v_exp_f32_e32 v28, v28
	v_exp_f32_e32 v29, v29
	v_exp_f32_e32 v30, v30
	v_exp_f32_e32 v31, v31
	v_exp_f32_e32 v32, v32
	v_cvt_pk_bf16_f32 v12, v33, v34
	v_cvt_pk_bf16_f32 v13, v35, v36
	v_cvt_pk_bf16_f32 v14, v37, v38
	v_cvt_pk_bf16_f32 v15, v39, v40
	v_add_f32_e32 v33, 0, v33
	v_cvt_pk_bf16_f32 v16, v41, v42
	v_cvt_pk_bf16_f32 v17, v43, v44
	v_cvt_pk_bf16_f32 v18, v45, v46
	v_cvt_pk_bf16_f32 v19, v47, v91
	v_cvt_pk_bf16_f32 v20, v92, v93
	v_cvt_pk_bf16_f32 v21, v94, v95
	v_cvt_pk_bf16_f32 v22, v99, v100
	v_cvt_pk_bf16_f32 v23, v101, v102
	v_cvt_pk_bf16_f32 v24, v103, v104
	v_cvt_pk_bf16_f32 v25, v105, v28
	v_cvt_pk_bf16_f32 v26, v29, v30
	v_cvt_pk_bf16_f32 v27, v31, v32
	ds_write_b128 v89, v[12:15]
	ds_write_b128 v89, v[16:19] offset:1024
	ds_write_b128 v89, v[20:23] offset:2048
	ds_write_b128 v89, v[24:27] offset:3072
	v_add_f32_e32 v12, v33, v34
	v_add_f32_e32 v12, v12, v35
	v_add_f32_e32 v12, v12, v36
	v_add_f32_e32 v12, v12, v37
	v_add_f32_e32 v12, v12, v38
	v_add_f32_e32 v12, v12, v39
	v_add_f32_e32 v12, v12, v40
	v_add_f32_e32 v12, v12, v41
	v_add_f32_e32 v12, v12, v42
	v_add_f32_e32 v12, v12, v43
	v_add_f32_e32 v12, v12, v44
	v_add_f32_e32 v12, v12, v45
	v_add_f32_e32 v12, v12, v46
	v_add_f32_e32 v12, v12, v47
	v_add_f32_e32 v12, v12, v91
	v_add_f32_e32 v12, v12, v92
	v_add_f32_e32 v12, v12, v93
	v_add_f32_e32 v12, v12, v94
	v_add_f32_e32 v12, v12, v95
	v_add_f32_e32 v12, v12, v99
	v_add_f32_e32 v12, v12, v100
	v_add_f32_e32 v12, v12, v101
	v_add_f32_e32 v12, v12, v102
	v_add_f32_e32 v12, v12, v103
	v_add_f32_e32 v12, v12, v104
	v_add_f32_e32 v12, v12, v105
	v_add_f32_e32 v12, v12, v28
	v_add_f32_e32 v12, v12, v29
	v_add_f32_e32 v12, v12, v30
	s_waitcnt lgkmcnt(0)
	s_barrier
	v_add_f32_e32 v12, v12, v31
	v_xor_b32_e32 v0, 0x80000000, v90
	v_add_f32_e32 v12, v12, v32
	v_mov_b32_e32 v1, v0
	v_mov_b32_e32 v2, v0
	v_mov_b32_e32 v3, v0
	v_mov_b32_e32 v4, v0
	v_mov_b32_e32 v5, v0
	v_mov_b32_e32 v6, v0
	v_mov_b32_e32 v7, v0
	v_mov_b32_e32 v8, v0
	v_mov_b32_e32 v9, v0
	v_mov_b32_e32 v10, v0
	v_mov_b32_e32 v11, v0
	v_add_f32_e32 v99, 0, v12
	v_mov_b32_e32 v12, v0
	v_mov_b32_e32 v13, v0
	v_mov_b32_e32 v14, v0
	v_mov_b32_e32 v15, v0
	s_branch .LBB1_21

.LBB1_21:
	s_setprio 1
	v_add_u32_e32 v16, s5, v80
	ds_read_b128 v[32:35], v16
	ds_read_b128 v[36:39], v16 offset:256
	ds_read_b128 v[92:95], v16 offset:16384
	ds_read_b128 v[100:103], v16 offset:16640
	v_add_u32_e32 v16, s5, v81
	ds_read_b128 v[40:43], v16
	ds_read_b128 v[44:47], v16 offset:256
	ds_read_b128 v[104:107], v16 offset:16384
	ds_read_b128 v[108:111], v16 offset:16640
	s_waitcnt lgkmcnt(4)
	v_add_u32_e32 v91, s5, v82
	v_mfma_f32_32x32x16_bf16 v[16:31], v[32:35], v[128:131], v[0:15]
	ds_read_b128 v[32:35], v91
	v_mfma_f32_32x32x16_bf16 v[16:31], v[36:39], v[160:163], v[16:31]
	ds_read_b128 v[36:39], v91 offset:256
	ds_read_b128 v[112:115], v91 offset:16384
	ds_read_b128 v[116:119], v91 offset:16640
	s_waitcnt lgkmcnt(4)
	v_add_u32_e32 v91, s5, v83
	v_mfma_f32_32x32x16_bf16 v[16:31], v[40:43], v[132:135], v[16:31]
	ds_read_b128 v[40:43], v91
	v_mfma_f32_32x32x16_bf16 v[16:31], v[44:47], v[164:167], v[16:31]
	ds_read_b128 v[44:47], v91 offset:256
	ds_read_b128 v[120:123], v91 offset:16384
	ds_read_b128 v[124:127], v91 offset:16640
	s_waitcnt lgkmcnt(4)
	v_add_u32_e32 v91, s5, v84
	v_mfma_f32_32x32x16_bf16 v[16:31], v[32:35], v[136:139], v[16:31]
	ds_read_b128 v[32:35], v91
	v_mfma_f32_32x32x16_bf16 v[16:31], v[36:39], v[168:171], v[16:31]
	ds_read_b128 v[36:39], v91 offset:256
	ds_read_b128 v[194:197], v91 offset:16384
	ds_read_b128 v[198:201], v91 offset:16640
	s_waitcnt lgkmcnt(4)
	v_add_u32_e32 v91, s5, v85
	v_mfma_f32_32x32x16_bf16 v[16:31], v[40:43], v[140:143], v[16:31]
	ds_read_b128 v[40:43], v91
	v_mfma_f32_32x32x16_bf16 v[16:31], v[44:47], v[172:175], v[16:31]
	ds_read_b128 v[44:47], v91 offset:256
	ds_read_b128 v[202:205], v91 offset:16384
	ds_read_b128 v[206:209], v91 offset:16640
	s_waitcnt lgkmcnt(4)
	v_add_u32_e32 v91, s5, v86
	v_mfma_f32_32x32x16_bf16 v[16:31], v[32:35], v[144:147], v[16:31]
	ds_read_b128 v[32:35], v91
	v_mfma_f32_32x32x16_bf16 v[16:31], v[36:39], v[176:179], v[16:31]
	ds_read_b128 v[36:39], v91 offset:256
	ds_read_b128 v[210:213], v91 offset:16384
	ds_read_b128 v[214:217], v91 offset:16640
	s_waitcnt lgkmcnt(4)
	v_add_u32_e32 v91, s5, v87
	v_mfma_f32_32x32x16_bf16 v[16:31], v[40:43], v[148:151], v[16:31]
	ds_read_b128 v[40:43], v91
	v_mfma_f32_32x32x16_bf16 v[16:31], v[44:47], v[180:183], v[16:31]
	ds_read_b128 v[44:47], v91 offset:256
	ds_read_b128 v[218:221], v91 offset:16384
	ds_read_b128 v[222:225], v91 offset:16640
	s_waitcnt lgkmcnt(4)
	s_nop 0
	s_waitcnt lgkmcnt(0)
	v_mfma_f32_32x32x16_bf16 v[16:31], v[32:35], v[152:155], v[16:31]
	v_mfma_f32_32x32x16_bf16 v[16:31], v[36:39], v[184:187], v[16:31]
	v_mfma_f32_32x32x16_bf16 v[16:31], v[40:43], v[156:159], v[16:31]
	v_mfma_f32_32x32x16_bf16 v[16:31], v[44:47], v[188:191], v[16:31]
	v_mfma_f32_32x32x16_bf16 v[32:47], v[92:95], v[128:131], v[0:15]
	s_and_b32 s13, s11, 1
	s_nop 9
	v_max_f32_e32 v91, v17, v17
	v_max_f32_e32 v92, v16, v16
	v_max_f32_e32 v91, v92, v91
	v_max3_f32 v91, v91, v18, v19
	v_max3_f32 v91, v91, v20, v21
	v_max3_f32 v91, v91, v22, v23
	v_max3_f32 v91, v91, v24, v25
	v_max3_f32 v91, v91, v26, v27
	v_mfma_f32_32x32x16_bf16 v[32:47], v[100:103], v[160:163], v[32:47]
	v_max3_f32 v91, v91, v28, v29
	v_max3_f32 v91, v91, v30, v31
	v_mfma_f32_32x32x16_bf16 v[32:47], v[104:107], v[132:135], v[32:47]
	v_mfma_f32_32x32x16_bf16 v[32:47], v[108:111], v[164:167], v[32:47]
	v_mfma_f32_32x32x16_bf16 v[32:47], v[112:115], v[136:139], v[32:47]
	v_mfma_f32_32x32x16_bf16 v[32:47], v[116:119], v[168:171], v[32:47]
	v_mfma_f32_32x32x16_bf16 v[32:47], v[120:123], v[140:143], v[32:47]
	v_mfma_f32_32x32x16_bf16 v[32:47], v[124:127], v[172:175], v[32:47]
	v_mfma_f32_32x32x16_bf16 v[32:47], v[194:197], v[144:147], v[32:47]
	v_mfma_f32_32x32x16_bf16 v[32:47], v[198:201], v[176:179], v[32:47]
	v_mfma_f32_32x32x16_bf16 v[32:47], v[202:205], v[148:151], v[32:47]
	v_mfma_f32_32x32x16_bf16 v[32:47], v[206:209], v[180:183], v[32:47]
	v_mfma_f32_32x32x16_bf16 v[32:47], v[210:213], v[152:155], v[32:47]
	v_mfma_f32_32x32x16_bf16 v[32:47], v[214:217], v[184:187], v[32:47]
	v_mfma_f32_32x32x16_bf16 v[32:47], v[218:221], v[156:159], v[32:47]
	v_mfma_f32_32x32x16_bf16 v[32:47], v[222:225], v[188:191], v[32:47]
	s_setprio 0
	s_nop 10
	v_max3_f32 v91, v91, v32, v33
	v_max3_f32 v91, v91, v34, v35
	v_max3_f32 v91, v91, v36, v37
	v_max3_f32 v91, v91, v38, v39
	v_max3_f32 v91, v91, v40, v41
	v_max3_f32 v91, v91, v42, v43
	v_max3_f32 v91, v91, v44, v45
	v_max3_f32 v91, v91, v46, v47
	v_mov_b32_e32 v92, v91
	s_nop 1
	v_permlane32_swap_b32_e32 v91, v92
	v_max_f32_e32 v92, v92, v92
	v_max_f32_e32 v91, v91, v91
	v_max_f32_e32 v91, v91, v92
	v_cmp_ge_f32_e32 vcc, s12, v91
	s_cmp_eq_u64 vcc, exec
	s_cbranch_scc0 .LBB1_19
	s_mov_b32 s14, 0
	s_branch .LBB1_20

	.amdhsa_kernel _Z12fused_kernelPKtS0_PKfS0_S2_S2_Pf
		.amdhsa_group_segment_fixed_size 0
		.amdhsa_private_segment_fixed_size 0
		.amdhsa_kernarg_size 56
		.amdhsa_user_sgpr_count 2
		.amdhsa_user_sgpr_dispatch_ptr 0
		.amdhsa_user_sgpr_queue_ptr 0
		.amdhsa_user_sgpr_kernarg_segment_ptr 1
		.amdhsa_user_sgpr_dispatch_id 0
		.amdhsa_user_sgpr_kernarg_preload_length 0
		.amdhsa_user_sgpr_kernarg_preload_offset 0
		.amdhsa_user_sgpr_private_segment_size 0
		.amdhsa_uses_dynamic_stack 0
		.amdhsa_enable_private_segment 0
		.amdhsa_system_sgpr_workgroup_id_x 1
		.amdhsa_system_sgpr_workgroup_id_y 0
		.amdhsa_system_sgpr_workgroup_id_z 0
		.amdhsa_system_sgpr_workgroup_info 0
		.amdhsa_system_vgpr_workitem_id 0
		.amdhsa_next_free_vgpr 248
		.amdhsa_next_free_sgpr 40
		.amdhsa_accum_offset 248
		.amdhsa_reserve_vcc 1
		.amdhsa_float_round_mode_32 0
		.amdhsa_float_round_mode_16_64 0
		.amdhsa_float_denorm_mode_32 3
		.amdhsa_float_denorm_mode_16_64 3
		.amdhsa_dx10_clamp 1
		.amdhsa_ieee_mode 1
		.amdhsa_fp16_overflow 0
		.amdhsa_tg_split 0
		.amdhsa_exception_fp_ieee_invalid_op 0
		.amdhsa_exception_fp_denorm_src 0
		.amdhsa_exception_fp_ieee_div_zero 0
		.amdhsa_exception_fp_ieee_overflow 0
		.amdhsa_exception_fp_ieee_underflow 0
		.amdhsa_exception_fp_ieee_inexact 0
		.amdhsa_exception_int_div_zero 0
	.end_amdhsa_kernel

amdhsa.kernels:
  - .agpr_count:     0
    .args:
      - .actual_access:  read_only
        .address_space:  global
        .offset:         0
        .size:           8
        .value_kind:     global_buffer
      - .actual_access:  read_only
        .address_space:  global
        .offset:         8
        .size:           8
        .value_kind:     global_buffer
      - .actual_access:  read_only
        .address_space:  global
        .offset:         16
        .size:           8
        .value_kind:     global_buffer
      - .actual_access:  read_only
        .address_space:  global
        .offset:         24
        .size:           8
        .value_kind:     global_buffer
      - .actual_access:  read_only
        .address_space:  global
        .offset:         32
        .size:           8
        .value_kind:     global_buffer
      - .address_space:  global
        .offset:         40
        .size:           8
        .value_kind:     global_buffer
      - .actual_access:  write_only
        .address_space:  global
        .offset:         48
        .size:           8
        .value_kind:     global_buffer
      - .actual_access:  write_only
        .address_space:  global
        .offset:         56
        .size:           8
        .value_kind:     global_buffer
      - .actual_access:  write_only
        .address_space:  global
        .offset:         64
        .size:           8
        .value_kind:     global_buffer
    .group_segment_fixed_size: 21520
    .kernarg_segment_align: 8
    .kernarg_segment_size: 72
    .language:       OpenCL C
    .language_version:
      - 2
      - 0
    .max_flat_workgroup_size: 256
    .name:           _Z11prep_kernelPKfS0_S0_S0_S0_PtS1_PfS1_
    .private_segment_fixed_size: 0
    .sgpr_count:     20
    .sgpr_spill_count: 0
    .symbol:         _Z11prep_kernelPKfS0_S0_S0_S0_PtS1_PfS1_.kd
    .uniform_work_group_size: 1
    .uses_dynamic_stack: false
    .vgpr_count:     70
    .vgpr_spill_count: 0
    .wavefront_size: 64
  - .agpr_count:     0
    .args:
      - .address_space:  global
        .offset:         0
        .size:           8
        .value_kind:     global_buffer
      - .address_space:  global
        .offset:         8
        .size:           8
        .value_kind:     global_buffer
      - .actual_access:  read_only
        .address_space:  global
        .offset:         16
        .size:           8
        .value_kind:     global_buffer
      - .address_space:  global
        .offset:         24
        .size:           8
        .value_kind:     global_buffer
      - .actual_access:  read_only
        .address_space:  global
        .offset:         32
        .size:           8
        .value_kind:     global_buffer
      - .actual_access:  read_only
        .address_space:  global
        .offset:         40
        .size:           8
        .value_kind:     global_buffer
      - .actual_access:  write_only
        .address_space:  global
        .offset:         48
        .size:           8
        .value_kind:     global_buffer
    .group_segment_fixed_size: 0
    .kernarg_segment_align: 8
    .kernarg_segment_size: 56
    .language:       OpenCL C
    .language_version:
      - 2
      - 0
    .max_flat_workgroup_size: 512
    .name:           _Z12fused_kernelPKtS0_PKfS0_S2_S2_Pf
    .private_segment_fixed_size: 0
    .sgpr_count:     46
    .sgpr_spill_count: 0
    .symbol:         _Z12fused_kernelPKtS0_PKfS0_S2_S2_Pf.kd
    .uniform_work_group_size: 1
    .uses_dynamic_stack: false
    .vgpr_count:     248
    .vgpr_spill_count: 0
    .wavefront_size: 64
